# v70 + P10 key-norm bound loop: loads of four trips issued together, one wait, then the four norm computations
# baseline (speedup 1.0000x reference)
.LBB0_1109:
	s_mov_b64 s[12:13], 0x1000
	s_mov_b64 s[2:3], exec
	v_max_f32_e32 v19, v19, v19
	v_ashrrev_i32_e32 v40, 6, v18
	v_ashrrev_i32_e32 v41, 31, v40
	v_and_b32_e32 v42, 0x1f8, v17
	v_lshlrev_b64 v[40:41], 13, v[40:41]
	v_lshlrev_b32_e32 v52, 1, v42
	v_lshl_add_u64 v[40:41], s[80:81], 0, v[40:41]
	v_lshl_add_u64 v[36:37], v[40:41], 0, v[52:53]
	global_load_dwordx4 v[66:69], v[36:37], off
	global_load_dwordx4 v[62:65], v[36:37], off offset:1024
	global_load_dwordx4 v[58:61], v[36:37], off offset:2048
	global_load_dwordx4 v[54:57], v[36:37], off offset:3072
	v_lshl_add_u64 v[38:39], v[36:37], 0, s[12:13]
	global_load_dwordx4 v[70:73], v[38:39], off offset:2048
	global_load_dwordx4 v[74:77], v[38:39], off
	global_load_dwordx4 v[78:81], v[38:39], off offset:1024
	global_load_dwordx4 v[82:85], v[38:39], off offset:3072
	v_add_u32_e32 v18, 0x200, v18
	v_add_u32_e32 v17, 0x1000, v17
	v_cmp_le_i32_e32 vcc, s0, v18
	s_andn2_b64 exec, exec, vcc
	s_mov_b64 s[4:5], exec
	v_ashrrev_i32_e32 v40, 6, v18
	v_ashrrev_i32_e32 v41, 31, v40
	v_and_b32_e32 v42, 0x1f8, v17
	v_lshlrev_b64 v[40:41], 13, v[40:41]
	v_lshlrev_b32_e32 v52, 1, v42
	v_lshl_add_u64 v[40:41], s[80:81], 0, v[40:41]
	v_lshl_add_u64 v[36:37], v[40:41], 0, v[52:53]
	global_load_dwordx4 v[98:101], v[36:37], off
	global_load_dwordx4 v[94:97], v[36:37], off offset:1024
	global_load_dwordx4 v[90:93], v[36:37], off offset:2048
	global_load_dwordx4 v[86:89], v[36:37], off offset:3072
	v_lshl_add_u64 v[38:39], v[36:37], 0, s[12:13]
	global_load_dwordx4 v[102:105], v[38:39], off offset:2048
	global_load_dwordx4 v[106:109], v[38:39], off
	global_load_dwordx4 v[110:113], v[38:39], off offset:1024
	global_load_dwordx4 v[114:117], v[38:39], off offset:3072
	v_add_u32_e32 v18, 0x200, v18
	v_add_u32_e32 v17, 0x1000, v17
	v_cmp_le_i32_e32 vcc, s0, v18
	s_andn2_b64 exec, exec, vcc
	s_mov_b64 s[6:7], exec
	v_ashrrev_i32_e32 v40, 6, v18
	v_ashrrev_i32_e32 v41, 31, v40
	v_and_b32_e32 v42, 0x1f8, v17
	v_lshlrev_b64 v[40:41], 13, v[40:41]
	v_lshlrev_b32_e32 v52, 1, v42
	v_lshl_add_u64 v[40:41], s[80:81], 0, v[40:41]
	v_lshl_add_u64 v[36:37], v[40:41], 0, v[52:53]
	global_load_dwordx4 v[200:203], v[36:37], off
	global_load_dwordx4 v[196:199], v[36:37], off offset:1024
	global_load_dwordx4 v[192:195], v[36:37], off offset:2048
	global_load_dwordx4 v[188:191], v[36:37], off offset:3072
	v_lshl_add_u64 v[38:39], v[36:37], 0, s[12:13]
	global_load_dwordx4 v[204:207], v[38:39], off offset:2048
	global_load_dwordx4 v[208:211], v[38:39], off
	global_load_dwordx4 v[212:215], v[38:39], off offset:1024
	global_load_dwordx4 v[216:219], v[38:39], off offset:3072
	v_add_u32_e32 v18, 0x200, v18
	v_add_u32_e32 v17, 0x1000, v17
	v_cmp_le_i32_e32 vcc, s0, v18
	s_andn2_b64 exec, exec, vcc
	s_mov_b64 s[8:9], exec
	v_ashrrev_i32_e32 v40, 6, v18
	v_ashrrev_i32_e32 v41, 31, v40
	v_and_b32_e32 v42, 0x1f8, v17
	v_lshlrev_b64 v[40:41], 13, v[40:41]
	v_lshlrev_b32_e32 v52, 1, v42
	v_lshl_add_u64 v[40:41], s[80:81], 0, v[40:41]
	v_lshl_add_u64 v[36:37], v[40:41], 0, v[52:53]
	global_load_dwordx4 v[130:133], v[36:37], off
	global_load_dwordx4 v[126:129], v[36:37], off offset:1024
	global_load_dwordx4 v[122:125], v[36:37], off offset:2048
	global_load_dwordx4 v[118:121], v[36:37], off offset:3072
	v_lshl_add_u64 v[38:39], v[36:37], 0, s[12:13]
	global_load_dwordx4 v[134:137], v[38:39], off offset:2048
	global_load_dwordx4 v[220:223], v[38:39], off
	global_load_dwordx4 v[224:227], v[38:39], off offset:1024
	global_load_dwordx4 v[228:231], v[38:39], off offset:3072
	v_add_u32_e32 v18, 0x200, v18
	v_add_u32_e32 v17, 0x1000, v17
	v_cmp_le_i32_e32 vcc, s0, v18
	s_andn2_b64 exec, exec, vcc
	s_mov_b64 s[10:11], exec
	s_waitcnt vmcnt(0)
	s_mov_b64 exec, s[2:3]
	v_cvt_f32_f16_sdwa v42, v66 dst_sel:DWORD dst_unused:UNUSED_PAD src0_sel:WORD_1
	v_mul_f32_e32 v42, v42, v42
	v_fma_mix_f32 v66, v66, v66, v42 op_sel_hi:[1,1,0]
	v_cvt_f32_f16_e32 v36, v72
	v_fma_mix_f32 v66, v67, v67, v66 op_sel_hi:[1,1,0]
	v_cvt_f32_f16_sdwa v37, v72 dst_sel:DWORD dst_unused:UNUSED_PAD src0_sel:WORD_1
	v_fma_mix_f32 v66, v67, v67, v66 op_sel:[1,1,0] op_sel_hi:[1,1,0]
	v_cvt_f32_f16_e32 v72, v73
	v_fma_mix_f32 v66, v68, v68, v66 op_sel_hi:[1,1,0]
	v_cvt_f32_f16_sdwa v73, v73 dst_sel:DWORD dst_unused:UNUSED_PAD src0_sel:WORD_1
	v_fma_mix_f32 v66, v68, v68, v66 op_sel:[1,1,0] op_sel_hi:[1,1,0]
	v_cvt_f32_f16_e32 v38, v82
	v_fma_mix_f32 v66, v69, v69, v66 op_sel_hi:[1,1,0]
	v_cvt_f32_f16_sdwa v39, v82 dst_sel:DWORD dst_unused:UNUSED_PAD src0_sel:WORD_1
	v_fma_mix_f32 v66, v69, v69, v66 op_sel:[1,1,0] op_sel_hi:[1,1,0]
	v_pk_mul_f32 v[36:37], v[36:37], v[36:37]
	v_fma_mix_f32 v66, v62, v62, v66 op_sel_hi:[1,1,0]
	v_cvt_f32_f16_e32 v82, v83
	v_fma_mix_f32 v62, v62, v62, v66 op_sel:[1,1,0] op_sel_hi:[1,1,0]
	v_cvt_f32_f16_sdwa v83, v83 dst_sel:DWORD dst_unused:UNUSED_PAD src0_sel:WORD_1
	v_fma_mix_f32 v62, v63, v63, v62 op_sel_hi:[1,1,0]
	v_pk_mul_f32 v[72:73], v[72:73], v[72:73]
	v_fma_mix_f32 v62, v63, v63, v62 op_sel:[1,1,0] op_sel_hi:[1,1,0]
	v_cvt_f32_f16_e32 v40, v84
	v_fma_mix_f32 v62, v64, v64, v62 op_sel_hi:[1,1,0]
	v_cvt_f32_f16_sdwa v41, v84 dst_sel:DWORD dst_unused:UNUSED_PAD src0_sel:WORD_1
	v_fma_mix_f32 v62, v64, v64, v62 op_sel:[1,1,0] op_sel_hi:[1,1,0]
	v_pk_mul_f32 v[38:39], v[38:39], v[38:39]
	v_fma_mix_f32 v62, v65, v65, v62 op_sel_hi:[1,1,0]
	v_cvt_f32_f16_e32 v84, v85
	v_fma_mix_f32 v62, v65, v65, v62 op_sel:[1,1,0] op_sel_hi:[1,1,0]
	v_cvt_f32_f16_sdwa v85, v85 dst_sel:DWORD dst_unused:UNUSED_PAD src0_sel:WORD_1
	v_fma_mix_f32 v62, v58, v58, v62 op_sel_hi:[1,1,0]
	v_pk_mul_f32 v[82:83], v[82:83], v[82:83]
	v_fma_mix_f32 v58, v58, v58, v62 op_sel:[1,1,0] op_sel_hi:[1,1,0]
	v_pk_mul_f32 v[40:41], v[40:41], v[40:41]
	v_fma_mix_f32 v58, v59, v59, v58 op_sel_hi:[1,1,0]
	v_pk_mul_f32 v[84:85], v[84:85], v[84:85]
	v_fma_mix_f32 v58, v59, v59, v58 op_sel:[1,1,0] op_sel_hi:[1,1,0]
	s_nop 0
	v_fma_mix_f32 v58, v60, v60, v58 op_sel_hi:[1,1,0]
	s_nop 0
	v_fma_mix_f32 v58, v60, v60, v58 op_sel:[1,1,0] op_sel_hi:[1,1,0]
	s_nop 0
	v_fma_mix_f32 v58, v61, v61, v58 op_sel_hi:[1,1,0]
	s_nop 0
	v_fma_mix_f32 v58, v61, v61, v58 op_sel:[1,1,0] op_sel_hi:[1,1,0]
	s_nop 0
	v_fma_mix_f32 v58, v54, v54, v58 op_sel_hi:[1,1,0]
	s_nop 0
	v_fma_mix_f32 v54, v54, v54, v58 op_sel:[1,1,0] op_sel_hi:[1,1,0]
	s_nop 0
	v_fma_mix_f32 v54, v55, v55, v54 op_sel_hi:[1,1,0]
	s_nop 0
	v_fma_mix_f32 v54, v55, v55, v54 op_sel:[1,1,0] op_sel_hi:[1,1,0]
	s_nop 0
	v_fma_mix_f32 v54, v56, v56, v54 op_sel_hi:[1,1,0]
	s_nop 0
	v_fma_mix_f32 v54, v56, v56, v54 op_sel:[1,1,0] op_sel_hi:[1,1,0]
	s_nop 0
	v_fma_mix_f32 v54, v57, v57, v54 op_sel_hi:[1,1,0]
	s_nop 0
	v_fma_mix_f32 v54, v57, v57, v54 op_sel:[1,1,0] op_sel_hi:[1,1,0]
	s_nop 0
	v_fma_mix_f32 v54, v74, v74, v54 op_sel_hi:[1,1,0]
	s_nop 0
	v_fma_mix_f32 v54, v74, v74, v54 op_sel:[1,1,0] op_sel_hi:[1,1,0]
	s_nop 0
	v_fma_mix_f32 v54, v75, v75, v54 op_sel_hi:[1,1,0]
	s_nop 0
	v_fma_mix_f32 v54, v75, v75, v54 op_sel:[1,1,0] op_sel_hi:[1,1,0]
	s_nop 0
	v_fma_mix_f32 v54, v76, v76, v54 op_sel_hi:[1,1,0]
	s_nop 0
	v_fma_mix_f32 v54, v76, v76, v54 op_sel:[1,1,0] op_sel_hi:[1,1,0]
	s_nop 0
	v_fma_mix_f32 v54, v77, v77, v54 op_sel_hi:[1,1,0]
	s_nop 0
	v_fma_mix_f32 v54, v77, v77, v54 op_sel:[1,1,0] op_sel_hi:[1,1,0]
	s_nop 0
	v_fma_mix_f32 v54, v78, v78, v54 op_sel_hi:[1,1,0]
	s_nop 0
	v_fma_mix_f32 v54, v78, v78, v54 op_sel:[1,1,0] op_sel_hi:[1,1,0]
	s_nop 0
	v_fma_mix_f32 v54, v79, v79, v54 op_sel_hi:[1,1,0]
	s_nop 0
	v_fma_mix_f32 v54, v79, v79, v54 op_sel:[1,1,0] op_sel_hi:[1,1,0]
	s_nop 0
	v_fma_mix_f32 v54, v80, v80, v54 op_sel_hi:[1,1,0]
	s_nop 0
	v_fma_mix_f32 v54, v80, v80, v54 op_sel:[1,1,0] op_sel_hi:[1,1,0]
	s_nop 0
	v_fma_mix_f32 v54, v81, v81, v54 op_sel_hi:[1,1,0]
	s_nop 0
	v_fma_mix_f32 v54, v81, v81, v54 op_sel:[1,1,0] op_sel_hi:[1,1,0]
	s_nop 0
	v_fma_mix_f32 v54, v70, v70, v54 op_sel_hi:[1,1,0]
	s_nop 0
	v_fma_mix_f32 v54, v70, v70, v54 op_sel:[1,1,0] op_sel_hi:[1,1,0]
	s_nop 0
	v_fma_mix_f32 v54, v71, v71, v54 op_sel_hi:[1,1,0]
	s_nop 0
	v_fma_mix_f32 v54, v71, v71, v54 op_sel:[1,1,0] op_sel_hi:[1,1,0]
	s_nop 0
	v_add_f32_e32 v54, v36, v54
	v_add_f32_e32 v54, v37, v54
	v_add_f32_e32 v54, v72, v54
	v_add_f32_e32 v54, v73, v54
	v_add_f32_e32 v54, v38, v54
	v_add_f32_e32 v54, v39, v54
	v_add_f32_e32 v54, v82, v54
	v_add_f32_e32 v54, v83, v54
	v_add_f32_e32 v54, v40, v54
	v_add_f32_e32 v54, v41, v54
	v_add_f32_e32 v54, v84, v54
	v_add_f32_e32 v54, v85, v54
	v_max_f32_e32 v19, v19, v54
	s_mov_b64 exec, s[4:5]
	v_cvt_f32_f16_sdwa v42, v98 dst_sel:DWORD dst_unused:UNUSED_PAD src0_sel:WORD_1
	v_mul_f32_e32 v42, v42, v42
	v_fma_mix_f32 v98, v98, v98, v42 op_sel_hi:[1,1,0]
	v_cvt_f32_f16_e32 v36, v104
	v_fma_mix_f32 v98, v99, v99, v98 op_sel_hi:[1,1,0]
	v_cvt_f32_f16_sdwa v37, v104 dst_sel:DWORD dst_unused:UNUSED_PAD src0_sel:WORD_1
	v_fma_mix_f32 v98, v99, v99, v98 op_sel:[1,1,0] op_sel_hi:[1,1,0]
	v_cvt_f32_f16_e32 v104, v105
	v_fma_mix_f32 v98, v100, v100, v98 op_sel_hi:[1,1,0]
	v_cvt_f32_f16_sdwa v105, v105 dst_sel:DWORD dst_unused:UNUSED_PAD src0_sel:WORD_1
	v_fma_mix_f32 v98, v100, v100, v98 op_sel:[1,1,0] op_sel_hi:[1,1,0]
	v_cvt_f32_f16_e32 v38, v114
	v_fma_mix_f32 v98, v101, v101, v98 op_sel_hi:[1,1,0]
	v_cvt_f32_f16_sdwa v39, v114 dst_sel:DWORD dst_unused:UNUSED_PAD src0_sel:WORD_1
	v_fma_mix_f32 v98, v101, v101, v98 op_sel:[1,1,0] op_sel_hi:[1,1,0]
	v_pk_mul_f32 v[36:37], v[36:37], v[36:37]
	v_fma_mix_f32 v98, v94, v94, v98 op_sel_hi:[1,1,0]
	v_cvt_f32_f16_e32 v114, v115
	v_fma_mix_f32 v94, v94, v94, v98 op_sel:[1,1,0] op_sel_hi:[1,1,0]
	v_cvt_f32_f16_sdwa v115, v115 dst_sel:DWORD dst_unused:UNUSED_PAD src0_sel:WORD_1
	v_fma_mix_f32 v94, v95, v95, v94 op_sel_hi:[1,1,0]
	v_pk_mul_f32 v[104:105], v[104:105], v[104:105]
	v_fma_mix_f32 v94, v95, v95, v94 op_sel:[1,1,0] op_sel_hi:[1,1,0]
	v_cvt_f32_f16_e32 v40, v116
	v_fma_mix_f32 v94, v96, v96, v94 op_sel_hi:[1,1,0]
	v_cvt_f32_f16_sdwa v41, v116 dst_sel:DWORD dst_unused:UNUSED_PAD src0_sel:WORD_1
	v_fma_mix_f32 v94, v96, v96, v94 op_sel:[1,1,0] op_sel_hi:[1,1,0]
	v_pk_mul_f32 v[38:39], v[38:39], v[38:39]
	v_fma_mix_f32 v94, v97, v97, v94 op_sel_hi:[1,1,0]
	v_cvt_f32_f16_e32 v116, v117
	v_fma_mix_f32 v94, v97, v97, v94 op_sel:[1,1,0] op_sel_hi:[1,1,0]
	v_cvt_f32_f16_sdwa v117, v117 dst_sel:DWORD dst_unused:UNUSED_PAD src0_sel:WORD_1
	v_fma_mix_f32 v94, v90, v90, v94 op_sel_hi:[1,1,0]
	v_pk_mul_f32 v[114:115], v[114:115], v[114:115]
	v_fma_mix_f32 v90, v90, v90, v94 op_sel:[1,1,0] op_sel_hi:[1,1,0]
	v_pk_mul_f32 v[40:41], v[40:41], v[40:41]
	v_fma_mix_f32 v90, v91, v91, v90 op_sel_hi:[1,1,0]
	v_pk_mul_f32 v[116:117], v[116:117], v[116:117]
	v_fma_mix_f32 v90, v91, v91, v90 op_sel:[1,1,0] op_sel_hi:[1,1,0]
	s_nop 0
	v_fma_mix_f32 v90, v92, v92, v90 op_sel_hi:[1,1,0]
	s_nop 0
	v_fma_mix_f32 v90, v92, v92, v90 op_sel:[1,1,0] op_sel_hi:[1,1,0]
	s_nop 0
	v_fma_mix_f32 v90, v93, v93, v90 op_sel_hi:[1,1,0]
	s_nop 0
	v_fma_mix_f32 v90, v93, v93, v90 op_sel:[1,1,0] op_sel_hi:[1,1,0]
	s_nop 0
	v_fma_mix_f32 v90, v86, v86, v90 op_sel_hi:[1,1,0]
	s_nop 0
	v_fma_mix_f32 v86, v86, v86, v90 op_sel:[1,1,0] op_sel_hi:[1,1,0]
	s_nop 0
	v_fma_mix_f32 v86, v87, v87, v86 op_sel_hi:[1,1,0]
	s_nop 0
	v_fma_mix_f32 v86, v87, v87, v86 op_sel:[1,1,0] op_sel_hi:[1,1,0]
	s_nop 0
	v_fma_mix_f32 v86, v88, v88, v86 op_sel_hi:[1,1,0]
	s_nop 0
	v_fma_mix_f32 v86, v88, v88, v86 op_sel:[1,1,0] op_sel_hi:[1,1,0]
	s_nop 0
	v_fma_mix_f32 v86, v89, v89, v86 op_sel_hi:[1,1,0]
	s_nop 0
	v_fma_mix_f32 v86, v89, v89, v86 op_sel:[1,1,0] op_sel_hi:[1,1,0]
	s_nop 0
	v_fma_mix_f32 v86, v106, v106, v86 op_sel_hi:[1,1,0]
	s_nop 0
	v_fma_mix_f32 v86, v106, v106, v86 op_sel:[1,1,0] op_sel_hi:[1,1,0]
	s_nop 0
	v_fma_mix_f32 v86, v107, v107, v86 op_sel_hi:[1,1,0]
	s_nop 0
	v_fma_mix_f32 v86, v107, v107, v86 op_sel:[1,1,0] op_sel_hi:[1,1,0]
	s_nop 0
	v_fma_mix_f32 v86, v108, v108, v86 op_sel_hi:[1,1,0]
	s_nop 0
	v_fma_mix_f32 v86, v108, v108, v86 op_sel:[1,1,0] op_sel_hi:[1,1,0]
	s_nop 0
	v_fma_mix_f32 v86, v109, v109, v86 op_sel_hi:[1,1,0]
	s_nop 0
	v_fma_mix_f32 v86, v109, v109, v86 op_sel:[1,1,0] op_sel_hi:[1,1,0]
	s_nop 0
	v_fma_mix_f32 v86, v110, v110, v86 op_sel_hi:[1,1,0]
	s_nop 0
	v_fma_mix_f32 v86, v110, v110, v86 op_sel:[1,1,0] op_sel_hi:[1,1,0]
	s_nop 0
	v_fma_mix_f32 v86, v111, v111, v86 op_sel_hi:[1,1,0]
	s_nop 0
	v_fma_mix_f32 v86, v111, v111, v86 op_sel:[1,1,0] op_sel_hi:[1,1,0]
	s_nop 0
	v_fma_mix_f32 v86, v112, v112, v86 op_sel_hi:[1,1,0]
	s_nop 0
	v_fma_mix_f32 v86, v112, v112, v86 op_sel:[1,1,0] op_sel_hi:[1,1,0]
	s_nop 0
	v_fma_mix_f32 v86, v113, v113, v86 op_sel_hi:[1,1,0]
	s_nop 0
	v_fma_mix_f32 v86, v113, v113, v86 op_sel:[1,1,0] op_sel_hi:[1,1,0]
	s_nop 0
	v_fma_mix_f32 v86, v102, v102, v86 op_sel_hi:[1,1,0]
	s_nop 0
	v_fma_mix_f32 v86, v102, v102, v86 op_sel:[1,1,0] op_sel_hi:[1,1,0]
	s_nop 0
	v_fma_mix_f32 v86, v103, v103, v86 op_sel_hi:[1,1,0]
	s_nop 0
	v_fma_mix_f32 v86, v103, v103, v86 op_sel:[1,1,0] op_sel_hi:[1,1,0]
	s_nop 0
	v_add_f32_e32 v86, v36, v86
	v_add_f32_e32 v86, v37, v86
	v_add_f32_e32 v86, v104, v86
	v_add_f32_e32 v86, v105, v86
	v_add_f32_e32 v86, v38, v86
	v_add_f32_e32 v86, v39, v86
	v_add_f32_e32 v86, v114, v86
	v_add_f32_e32 v86, v115, v86
	v_add_f32_e32 v86, v40, v86
	v_add_f32_e32 v86, v41, v86
	v_add_f32_e32 v86, v116, v86
	v_add_f32_e32 v86, v117, v86
	v_max_f32_e32 v19, v19, v86
	s_mov_b64 exec, s[6:7]
	v_cvt_f32_f16_sdwa v42, v200 dst_sel:DWORD dst_unused:UNUSED_PAD src0_sel:WORD_1
	v_mul_f32_e32 v42, v42, v42
	v_fma_mix_f32 v200, v200, v200, v42 op_sel_hi:[1,1,0]
	v_cvt_f32_f16_e32 v36, v206
	v_fma_mix_f32 v200, v201, v201, v200 op_sel_hi:[1,1,0]
	v_cvt_f32_f16_sdwa v37, v206 dst_sel:DWORD dst_unused:UNUSED_PAD src0_sel:WORD_1
	v_fma_mix_f32 v200, v201, v201, v200 op_sel:[1,1,0] op_sel_hi:[1,1,0]
	v_cvt_f32_f16_e32 v206, v207
	v_fma_mix_f32 v200, v202, v202, v200 op_sel_hi:[1,1,0]
	v_cvt_f32_f16_sdwa v207, v207 dst_sel:DWORD dst_unused:UNUSED_PAD src0_sel:WORD_1
	v_fma_mix_f32 v200, v202, v202, v200 op_sel:[1,1,0] op_sel_hi:[1,1,0]
	v_cvt_f32_f16_e32 v38, v216
	v_fma_mix_f32 v200, v203, v203, v200 op_sel_hi:[1,1,0]
	v_cvt_f32_f16_sdwa v39, v216 dst_sel:DWORD dst_unused:UNUSED_PAD src0_sel:WORD_1
	v_fma_mix_f32 v200, v203, v203, v200 op_sel:[1,1,0] op_sel_hi:[1,1,0]
	v_pk_mul_f32 v[36:37], v[36:37], v[36:37]
	v_fma_mix_f32 v200, v196, v196, v200 op_sel_hi:[1,1,0]
	v_cvt_f32_f16_e32 v216, v217
	v_fma_mix_f32 v196, v196, v196, v200 op_sel:[1,1,0] op_sel_hi:[1,1,0]
	v_cvt_f32_f16_sdwa v217, v217 dst_sel:DWORD dst_unused:UNUSED_PAD src0_sel:WORD_1
	v_fma_mix_f32 v196, v197, v197, v196 op_sel_hi:[1,1,0]
	v_pk_mul_f32 v[206:207], v[206:207], v[206:207]
	v_fma_mix_f32 v196, v197, v197, v196 op_sel:[1,1,0] op_sel_hi:[1,1,0]
	v_cvt_f32_f16_e32 v40, v218
	v_fma_mix_f32 v196, v198, v198, v196 op_sel_hi:[1,1,0]
	v_cvt_f32_f16_sdwa v41, v218 dst_sel:DWORD dst_unused:UNUSED_PAD src0_sel:WORD_1
	v_fma_mix_f32 v196, v198, v198, v196 op_sel:[1,1,0] op_sel_hi:[1,1,0]
	v_pk_mul_f32 v[38:39], v[38:39], v[38:39]
	v_fma_mix_f32 v196, v199, v199, v196 op_sel_hi:[1,1,0]
	v_cvt_f32_f16_e32 v218, v219
	v_fma_mix_f32 v196, v199, v199, v196 op_sel:[1,1,0] op_sel_hi:[1,1,0]
	v_cvt_f32_f16_sdwa v219, v219 dst_sel:DWORD dst_unused:UNUSED_PAD src0_sel:WORD_1
	v_fma_mix_f32 v196, v192, v192, v196 op_sel_hi:[1,1,0]
	v_pk_mul_f32 v[216:217], v[216:217], v[216:217]
	v_fma_mix_f32 v192, v192, v192, v196 op_sel:[1,1,0] op_sel_hi:[1,1,0]
	v_pk_mul_f32 v[40:41], v[40:41], v[40:41]
	v_fma_mix_f32 v192, v193, v193, v192 op_sel_hi:[1,1,0]
	v_pk_mul_f32 v[218:219], v[218:219], v[218:219]
	v_fma_mix_f32 v192, v193, v193, v192 op_sel:[1,1,0] op_sel_hi:[1,1,0]
	s_nop 0
	v_fma_mix_f32 v192, v194, v194, v192 op_sel_hi:[1,1,0]
	s_nop 0
	v_fma_mix_f32 v192, v194, v194, v192 op_sel:[1,1,0] op_sel_hi:[1,1,0]
	s_nop 0
	v_fma_mix_f32 v192, v195, v195, v192 op_sel_hi:[1,1,0]
	s_nop 0
	v_fma_mix_f32 v192, v195, v195, v192 op_sel:[1,1,0] op_sel_hi:[1,1,0]
	s_nop 0
	v_fma_mix_f32 v192, v188, v188, v192 op_sel_hi:[1,1,0]
	s_nop 0
	v_fma_mix_f32 v188, v188, v188, v192 op_sel:[1,1,0] op_sel_hi:[1,1,0]
	s_nop 0
	v_fma_mix_f32 v188, v189, v189, v188 op_sel_hi:[1,1,0]
	s_nop 0
	v_fma_mix_f32 v188, v189, v189, v188 op_sel:[1,1,0] op_sel_hi:[1,1,0]
	s_nop 0
	v_fma_mix_f32 v188, v190, v190, v188 op_sel_hi:[1,1,0]
	s_nop 0
	v_fma_mix_f32 v188, v190, v190, v188 op_sel:[1,1,0] op_sel_hi:[1,1,0]
	s_nop 0
	v_fma_mix_f32 v188, v191, v191, v188 op_sel_hi:[1,1,0]
	s_nop 0
	v_fma_mix_f32 v188, v191, v191, v188 op_sel:[1,1,0] op_sel_hi:[1,1,0]
	s_nop 0
	v_fma_mix_f32 v188, v208, v208, v188 op_sel_hi:[1,1,0]
	s_nop 0
	v_fma_mix_f32 v188, v208, v208, v188 op_sel:[1,1,0] op_sel_hi:[1,1,0]
	s_nop 0
	v_fma_mix_f32 v188, v209, v209, v188 op_sel_hi:[1,1,0]
	s_nop 0
	v_fma_mix_f32 v188, v209, v209, v188 op_sel:[1,1,0] op_sel_hi:[1,1,0]
	s_nop 0
	v_fma_mix_f32 v188, v210, v210, v188 op_sel_hi:[1,1,0]
	s_nop 0
	v_fma_mix_f32 v188, v210, v210, v188 op_sel:[1,1,0] op_sel_hi:[1,1,0]
	s_nop 0
	v_fma_mix_f32 v188, v211, v211, v188 op_sel_hi:[1,1,0]
	s_nop 0
	v_fma_mix_f32 v188, v211, v211, v188 op_sel:[1,1,0] op_sel_hi:[1,1,0]
	s_nop 0
	v_fma_mix_f32 v188, v212, v212, v188 op_sel_hi:[1,1,0]
	s_nop 0
	v_fma_mix_f32 v188, v212, v212, v188 op_sel:[1,1,0] op_sel_hi:[1,1,0]
	s_nop 0
	v_fma_mix_f32 v188, v213, v213, v188 op_sel_hi:[1,1,0]
	s_nop 0
	v_fma_mix_f32 v188, v213, v213, v188 op_sel:[1,1,0] op_sel_hi:[1,1,0]
	s_nop 0
	v_fma_mix_f32 v188, v214, v214, v188 op_sel_hi:[1,1,0]
	s_nop 0
	v_fma_mix_f32 v188, v214, v214, v188 op_sel:[1,1,0] op_sel_hi:[1,1,0]
	s_nop 0
	v_fma_mix_f32 v188, v215, v215, v188 op_sel_hi:[1,1,0]
	s_nop 0
	v_fma_mix_f32 v188, v215, v215, v188 op_sel:[1,1,0] op_sel_hi:[1,1,0]
	s_nop 0
	v_fma_mix_f32 v188, v204, v204, v188 op_sel_hi:[1,1,0]
	s_nop 0
	v_fma_mix_f32 v188, v204, v204, v188 op_sel:[1,1,0] op_sel_hi:[1,1,0]
	s_nop 0
	v_fma_mix_f32 v188, v205, v205, v188 op_sel_hi:[1,1,0]
	s_nop 0
	v_fma_mix_f32 v188, v205, v205, v188 op_sel:[1,1,0] op_sel_hi:[1,1,0]
	s_nop 0
	v_add_f32_e32 v188, v36, v188
	v_add_f32_e32 v188, v37, v188
	v_add_f32_e32 v188, v206, v188
	v_add_f32_e32 v188, v207, v188
	v_add_f32_e32 v188, v38, v188
	v_add_f32_e32 v188, v39, v188
	v_add_f32_e32 v188, v216, v188
	v_add_f32_e32 v188, v217, v188
	v_add_f32_e32 v188, v40, v188
	v_add_f32_e32 v188, v41, v188
	v_add_f32_e32 v188, v218, v188
	v_add_f32_e32 v188, v219, v188
	v_max_f32_e32 v19, v19, v188
	s_mov_b64 exec, s[8:9]
	v_cvt_f32_f16_sdwa v42, v130 dst_sel:DWORD dst_unused:UNUSED_PAD src0_sel:WORD_1
	v_mul_f32_e32 v42, v42, v42
	v_fma_mix_f32 v130, v130, v130, v42 op_sel_hi:[1,1,0]
	v_cvt_f32_f16_e32 v36, v136
	v_fma_mix_f32 v130, v131, v131, v130 op_sel_hi:[1,1,0]
	v_cvt_f32_f16_sdwa v37, v136 dst_sel:DWORD dst_unused:UNUSED_PAD src0_sel:WORD_1
	v_fma_mix_f32 v130, v131, v131, v130 op_sel:[1,1,0] op_sel_hi:[1,1,0]
	v_cvt_f32_f16_e32 v136, v137
	v_fma_mix_f32 v130, v132, v132, v130 op_sel_hi:[1,1,0]
	v_cvt_f32_f16_sdwa v137, v137 dst_sel:DWORD dst_unused:UNUSED_PAD src0_sel:WORD_1
	v_fma_mix_f32 v130, v132, v132, v130 op_sel:[1,1,0] op_sel_hi:[1,1,0]
	v_cvt_f32_f16_e32 v38, v228
	v_fma_mix_f32 v130, v133, v133, v130 op_sel_hi:[1,1,0]
	v_cvt_f32_f16_sdwa v39, v228 dst_sel:DWORD dst_unused:UNUSED_PAD src0_sel:WORD_1
	v_fma_mix_f32 v130, v133, v133, v130 op_sel:[1,1,0] op_sel_hi:[1,1,0]
	v_pk_mul_f32 v[36:37], v[36:37], v[36:37]
	v_fma_mix_f32 v130, v126, v126, v130 op_sel_hi:[1,1,0]
	v_cvt_f32_f16_e32 v228, v229
	v_fma_mix_f32 v126, v126, v126, v130 op_sel:[1,1,0] op_sel_hi:[1,1,0]
	v_cvt_f32_f16_sdwa v229, v229 dst_sel:DWORD dst_unused:UNUSED_PAD src0_sel:WORD_1
	v_fma_mix_f32 v126, v127, v127, v126 op_sel_hi:[1,1,0]
	v_pk_mul_f32 v[136:137], v[136:137], v[136:137]
	v_fma_mix_f32 v126, v127, v127, v126 op_sel:[1,1,0] op_sel_hi:[1,1,0]
	v_cvt_f32_f16_e32 v40, v230
	v_fma_mix_f32 v126, v128, v128, v126 op_sel_hi:[1,1,0]
	v_cvt_f32_f16_sdwa v41, v230 dst_sel:DWORD dst_unused:UNUSED_PAD src0_sel:WORD_1
	v_fma_mix_f32 v126, v128, v128, v126 op_sel:[1,1,0] op_sel_hi:[1,1,0]
	v_pk_mul_f32 v[38:39], v[38:39], v[38:39]
	v_fma_mix_f32 v126, v129, v129, v126 op_sel_hi:[1,1,0]
	v_cvt_f32_f16_e32 v230, v231
	v_fma_mix_f32 v126, v129, v129, v126 op_sel:[1,1,0] op_sel_hi:[1,1,0]
	v_cvt_f32_f16_sdwa v231, v231 dst_sel:DWORD dst_unused:UNUSED_PAD src0_sel:WORD_1
	v_fma_mix_f32 v126, v122, v122, v126 op_sel_hi:[1,1,0]
	v_pk_mul_f32 v[228:229], v[228:229], v[228:229]
	v_fma_mix_f32 v122, v122, v122, v126 op_sel:[1,1,0] op_sel_hi:[1,1,0]
	v_pk_mul_f32 v[40:41], v[40:41], v[40:41]
	v_fma_mix_f32 v122, v123, v123, v122 op_sel_hi:[1,1,0]
	v_pk_mul_f32 v[230:231], v[230:231], v[230:231]
	v_fma_mix_f32 v122, v123, v123, v122 op_sel:[1,1,0] op_sel_hi:[1,1,0]
	s_nop 0
	v_fma_mix_f32 v122, v124, v124, v122 op_sel_hi:[1,1,0]
	s_nop 0
	v_fma_mix_f32 v122, v124, v124, v122 op_sel:[1,1,0] op_sel_hi:[1,1,0]
	s_nop 0
	v_fma_mix_f32 v122, v125, v125, v122 op_sel_hi:[1,1,0]
	s_nop 0
	v_fma_mix_f32 v122, v125, v125, v122 op_sel:[1,1,0] op_sel_hi:[1,1,0]
	s_nop 0
	v_fma_mix_f32 v122, v118, v118, v122 op_sel_hi:[1,1,0]
	s_nop 0
	v_fma_mix_f32 v118, v118, v118, v122 op_sel:[1,1,0] op_sel_hi:[1,1,0]
	s_nop 0
	v_fma_mix_f32 v118, v119, v119, v118 op_sel_hi:[1,1,0]
	s_nop 0
	v_fma_mix_f32 v118, v119, v119, v118 op_sel:[1,1,0] op_sel_hi:[1,1,0]
	s_nop 0
	v_fma_mix_f32 v118, v120, v120, v118 op_sel_hi:[1,1,0]
	s_nop 0
	v_fma_mix_f32 v118, v120, v120, v118 op_sel:[1,1,0] op_sel_hi:[1,1,0]
	s_nop 0
	v_fma_mix_f32 v118, v121, v121, v118 op_sel_hi:[1,1,0]
	s_nop 0
	v_fma_mix_f32 v118, v121, v121, v118 op_sel:[1,1,0] op_sel_hi:[1,1,0]
	s_nop 0
	v_fma_mix_f32 v118, v220, v220, v118 op_sel_hi:[1,1,0]
	s_nop 0
	v_fma_mix_f32 v118, v220, v220, v118 op_sel:[1,1,0] op_sel_hi:[1,1,0]
	s_nop 0
	v_fma_mix_f32 v118, v221, v221, v118 op_sel_hi:[1,1,0]
	s_nop 0
	v_fma_mix_f32 v118, v221, v221, v118 op_sel:[1,1,0] op_sel_hi:[1,1,0]
	s_nop 0
	v_fma_mix_f32 v118, v222, v222, v118 op_sel_hi:[1,1,0]
	s_nop 0
	v_fma_mix_f32 v118, v222, v222, v118 op_sel:[1,1,0] op_sel_hi:[1,1,0]
	s_nop 0
	v_fma_mix_f32 v118, v223, v223, v118 op_sel_hi:[1,1,0]
	s_nop 0
	v_fma_mix_f32 v118, v223, v223, v118 op_sel:[1,1,0] op_sel_hi:[1,1,0]
	s_nop 0
	v_fma_mix_f32 v118, v224, v224, v118 op_sel_hi:[1,1,0]
	s_nop 0
	v_fma_mix_f32 v118, v224, v224, v118 op_sel:[1,1,0] op_sel_hi:[1,1,0]
	s_nop 0
	v_fma_mix_f32 v118, v225, v225, v118 op_sel_hi:[1,1,0]
	s_nop 0
	v_fma_mix_f32 v118, v225, v225, v118 op_sel:[1,1,0] op_sel_hi:[1,1,0]
	s_nop 0
	v_fma_mix_f32 v118, v226, v226, v118 op_sel_hi:[1,1,0]
	s_nop 0
	v_fma_mix_f32 v118, v226, v226, v118 op_sel:[1,1,0] op_sel_hi:[1,1,0]
	s_nop 0
	v_fma_mix_f32 v118, v227, v227, v118 op_sel_hi:[1,1,0]
	s_nop 0
	v_fma_mix_f32 v118, v227, v227, v118 op_sel:[1,1,0] op_sel_hi:[1,1,0]
	s_nop 0
	v_fma_mix_f32 v118, v134, v134, v118 op_sel_hi:[1,1,0]
	s_nop 0
	v_fma_mix_f32 v118, v134, v134, v118 op_sel:[1,1,0] op_sel_hi:[1,1,0]
	s_nop 0
	v_fma_mix_f32 v118, v135, v135, v118 op_sel_hi:[1,1,0]
	s_nop 0
	v_fma_mix_f32 v118, v135, v135, v118 op_sel:[1,1,0] op_sel_hi:[1,1,0]
	s_nop 0
	v_add_f32_e32 v118, v36, v118
	v_add_f32_e32 v118, v37, v118
	v_add_f32_e32 v118, v136, v118
	v_add_f32_e32 v118, v137, v118
	v_add_f32_e32 v118, v38, v118
	v_add_f32_e32 v118, v39, v118
	v_add_f32_e32 v118, v228, v118
	v_add_f32_e32 v118, v229, v118
	v_add_f32_e32 v118, v40, v118
	v_add_f32_e32 v118, v41, v118
	v_add_f32_e32 v118, v230, v118
	v_add_f32_e32 v118, v231, v118
	v_max_f32_e32 v19, v19, v118
	s_mov_b64 exec, s[10:11]
	s_cbranch_execnz .LBB0_1109
	s_or_b64 exec, exec, s[52:53]
